# P11 epilogue: row scale pre-multiplied by -log2e (128 multiplies removed), the PE 1/8 folded into rcp(8e+8) (62 packed multiplies removed)
# baseline (speedup 1.0000x reference)
.LBB0_1079:
	s_add_u32 s47, s88, 0xfc00000
	s_addc_u32 s48, s89, 0
	s_add_u32 s12, s88, 0x510000
	s_addc_u32 s13, s89, 0
	s_ashr_i32 s49, s76, 31
	s_ashr_i32 s50, s30, 31
	s_add_u32 s51, s86, 0x5000000
	s_addc_u32 s52, s87, 0
	s_lshl_b32 s2, s2, 5
	s_mov_b64 s[14:15], 0x80
	s_and_b32 s18, s2, 0x60
	s_add_i32 m0, s37, 0x18000
	v_lshl_add_u64 v[6:7], v[6:7], 0, s[14:15]
	s_lshl_b32 s16, s5, 13
	s_lshl_b32 s17, s18, 7
	s_waitcnt vmcnt(2)
	s_barrier
	global_load_lds_dwordx4 v[6:7], off
	v_lshl_add_u64 v[4:5], v[4:5], 0, s[14:15]
	s_add_i32 m0, s37, 0x1a000
	s_add_i32 s53, s37, 0x8000
	s_add_i32 s54, s37, 0xa000
	global_load_lds_dwordx4 v[4:5], off
	v_lshl_add_u64 v[0:1], v[0:1], 0, s[14:15]
	s_mov_b32 m0, s53
	s_add_u32 s2, s20, 0x40080
	global_load_lds_dwordx4 v[0:1], off
	v_lshl_add_u64 v[0:1], v[2:3], 0, s[14:15]
	s_mov_b32 m0, s54
	s_addc_u32 s3, s21, 0
	global_load_lds_dwordx4 v[0:1], off
	s_add_i32 m0, s37, 0x1c000
	v_lshl_add_u64 v[0:1], s[2:3], 0, v[154:155]
	global_load_lds_dwordx4 v[0:1], off
	v_lshl_add_u64 v[0:1], s[2:3], 0, v[158:159]
	s_add_i32 m0, s37, 0x1e000
	v_lshlrev_b32_e32 v3, 6, v236
	global_load_lds_dwordx4 v[0:1], off
	v_bfe_u32 v1, v236, 4, 2
	v_lshlrev_b32_e32 v2, 4, v1
	s_movk_i32 s2, 0x3c0
	v_and_b32_e32 v0, 15, v236
	v_and_or_b32 v3, v3, s2, v2
	v_cmp_eq_u32_e64 s[2:3], 0, v1
	v_lshl_or_b32 v235, v1, 3, s18
	v_lshlrev_b32_e32 v1, 8, v236
	v_lshl_or_b32 v223, s5, 6, v0
	v_lshl_or_b32 v0, v0, 6, v2
	v_and_b32_e32 v1, 0x38000, v1
	v_lshlrev_b32_e32 v2, 11, v10
	v_lshlrev_b32_e32 v4, 2, v236
	v_or3_b32 v1, v8, v1, v2
	v_and_b32_e32 v4, 32, v4
	v_add_u32_e32 v160, v1, v9
	v_lshlrev_b32_e32 v1, 4, v11
	v_bitop3_b32 v0, v0, s16, v4 bitop3:0xde
	s_waitcnt vmcnt(6)
	s_cmpk_lt_u32 s4, 0x100
	v_and_b32_e32 v1, 0x78000, v1
	v_bitop3_b32 v234, s17, v3, v4 bitop3:0xf6
	s_cselect_b64 s[16:17], -1, 0
	v_or3_b32 v1, v8, v1, v2
	s_add_i32 s56, 0, 0x10000
	s_add_i32 s57, 0, 0x14000
	v_add_u32_e32 v239, 0, v0
	v_mbcnt_lo_u32_b32 v0, -1, 0
	s_mov_b32 s55, s76
	v_mov_b32_e32 v161, v155
	v_add_u32_e32 v162, v1, v9
	v_mov_b32_e32 v163, v155
	v_mov_b64_e32 v[164:165], 0x200
	v_mov_b64_e32 v[166:167], 0x1ff
	v_add_u32_e32 v237, s56, v234
	v_add_u32_e32 v238, s57, v234
	v_mbcnt_hi_u32_b32 v240, -1, v0
	v_mov_b32_e32 v252, 0x41000000
	s_barrier
	s_branch .LBB0_1082

.LBB0_1092:
	v_lshl_add_u32 v172, s36, 8, v223
	v_ashrrev_i32_e32 v173, 31, v172
	v_lshl_add_u64 v[180:181], v[172:173], 2, s[12:13]
	global_load_dword v220, v[180:181], off
	v_lshl_or_b32 v168, s38, 8, v235
	s_cmp_lt_i32 s36, 64
	s_cselect_b32 s21, s48, s52
	s_cselect_b32 s20, s47, s51
	v_ashrrev_i32_e32 v169, 31, v168
	v_lshl_add_u64 v[178:179], s[20:21], 0, v[168:169]
	v_lshlrev_b64 v[124:125], 10, v[172:173]
	v_lshl_add_u64 v[124:125], v[178:179], 0, v[124:125]
	global_load_dwordx2 v[224:225], v[124:125], off nt
	global_load_dwordx2 v[226:227], v[124:125], off offset:128 nt
	v_and_b32_e32 v127, 64, v240
	v_xor_b32_e32 v126, 16, v240
	v_add_u32_e32 v127, 64, v127
	v_lshlrev_b64 v[188:189], 1, v[168:169]
	v_xor_b32_e32 v128, 32, v240
	v_lshlrev_b64 v[190:191], 11, v[172:173]
	v_cmp_lt_i32_e32 vcc, v126, v127
	v_lshl_add_u64 v[192:193], s[8:9], 0, v[188:189]
	v_or_b32_e32 v184, 16, v172
	v_cndmask_b32_e32 v142, v240, v126, vcc
	v_cmp_lt_i32_e32 vcc, v128, v127
	v_lshl_add_u64 v[126:127], v[192:193], 0, v[190:191]
	global_load_dwordx4 v[212:215], v[126:127], off nt
	v_or_b32_e32 v174, 32, v172
	v_or_b32_e32 v170, 48, v172
	v_ashrrev_i32_e32 v185, 31, v184
	v_ashrrev_i32_e32 v175, 31, v174
	v_ashrrev_i32_e32 v171, 31, v170
	v_lshlrev_b64 v[130:131], 10, v[184:185]
	v_lshlrev_b64 v[186:187], 11, v[184:185]
	v_lshlrev_b64 v[138:139], 10, v[174:175]
	v_lshlrev_b64 v[182:183], 11, v[174:175]
	v_cndmask_b32_e32 v143, v240, v128, vcc
	v_lshl_add_u64 v[128:129], v[184:185], 2, s[12:13]
	v_lshl_add_u64 v[136:137], v[174:175], 2, s[12:13]
	v_lshl_add_u64 v[194:195], v[170:171], 2, s[12:13]
	v_lshlrev_b64 v[140:141], 10, v[170:171]
	v_lshlrev_b64 v[176:177], 11, v[170:171]
	v_lshl_add_u64 v[124:125], v[192:193], 0, v[186:187]
	v_lshl_add_u64 v[130:131], v[178:179], 0, v[130:131]
	v_lshl_add_u64 v[196:197], v[192:193], 0, v[182:183]
	v_lshl_add_u64 v[198:199], v[178:179], 0, v[138:139]
	v_lshlrev_b32_e32 v242, 2, v142
	v_lshlrev_b32_e32 v241, 2, v143
	v_lshl_add_u64 v[228:229], v[192:193], 0, v[176:177]
	v_lshl_add_u64 v[230:231], v[178:179], 0, v[140:141]
	global_load_dwordx4 v[216:219], v[126:127], off offset:256 nt
	global_load_dword v206, v[128:129], off
	global_load_dwordx4 v[148:151], v[124:125], off nt
	global_load_dwordx4 v[144:147], v[124:125], off offset:256 nt
	global_load_dwordx2 v[210:211], v[130:131], off nt
	global_load_dwordx2 v[204:205], v[130:131], off offset:128 nt
	global_load_dword v202, v[136:137], off
	global_load_dwordx4 v[140:143], v[196:197], off nt
	s_nop 0
	global_load_dwordx4 v[136:139], v[196:197], off offset:256 nt
	global_load_dwordx2 v[208:209], v[198:199], off nt
	global_load_dwordx2 v[200:201], v[198:199], off offset:128 nt
	s_nop 0
	global_load_dword v196, v[194:195], off
	global_load_dwordx4 v[128:131], v[228:229], off nt
	global_load_dwordx4 v[124:127], v[228:229], off offset:256 nt
	global_load_dwordx2 v[198:199], v[230:231], off nt
	s_nop 0
	global_load_dwordx2 v[194:195], v[230:231], off offset:128 nt
	s_waitcnt vmcnt(0)
	v_mul_f32_e32 v220, 0xbfb8aa3b, v220
	v_pk_mul_f32 v[120:121], v[120:121], v[220:221] op_sel_hi:[1,0]
	s_nop 0
	v_exp_f32_e32 v120, v120
	v_exp_f32_e32 v121, v121
	v_pk_mul_f32 v[132:133], v[132:133], v[220:221] op_sel_hi:[1,0]
	v_pk_mul_f32 v[134:135], v[134:135], v[220:221] op_sel_hi:[1,0]
	v_fmamk_f32 v120, v120, 0x41000000, v252
	v_pk_mul_f32 v[122:123], v[122:123], v[220:221] op_sel_hi:[1,0]
	v_exp_f32_e32 v197, v132
	v_exp_f32_e32 v203, v133
	v_rcp_f32_e32 v244, v120
	v_fmamk_f32 v120, v121, 0x41000000, v252
	v_exp_f32_e32 v134, v134
	v_exp_f32_e32 v135, v135
	v_rcp_f32_e32 v245, v120
	v_exp_f32_e32 v120, v122
	v_exp_f32_e32 v121, v123
	v_cvt_f32_fp8_e32 v228, v224
	v_cvt_f32_fp8_sdwa v229, v224 src0_sel:BYTE_1
	v_fmamk_f32 v197, v197, 0x41000000, v252
	v_fmamk_f32 v203, v203, 0x41000000, v252
	v_fmamk_f32 v207, v134, 0x41000000, v252
	v_fmamk_f32 v221, v135, 0x41000000, v252
	v_rcp_f32_e32 v134, v197
	v_rcp_f32_e32 v135, v203
	v_fmamk_f32 v120, v120, 0x41000000, v252
	v_cvt_f32_fp8_sdwa v132, v224 src0_sel:BYTE_2
	v_cvt_f32_fp8_sdwa v133, v224 src0_sel:BYTE_3
	v_rcp_f32_e32 v224, v120
	v_fmamk_f32 v120, v121, 0x41000000, v252
	v_pk_mul_f32 v[116:117], v[116:117], v[220:221] op_sel_hi:[1,0]
	v_cvt_f32_fp8_e32 v232, v225
	v_cvt_f32_fp8_sdwa v233, v225 src0_sel:BYTE_1
	v_cvt_f32_fp8_sdwa v122, v225 src0_sel:BYTE_2
	v_cvt_f32_fp8_sdwa v123, v225 src0_sel:BYTE_3
	v_rcp_f32_e32 v225, v120
	v_lshlrev_b32_e32 v120, 16, v212
	v_and_b32_e32 v121, 0xffff0000, v212
	v_pk_fma_f32 v[134:135], v[134:135], v[228:229], v[120:121]
	v_exp_f32_e32 v121, v116
	v_exp_f32_e32 v197, v117
	v_pk_mul_f32 v[118:119], v[118:119], v[220:221] op_sel_hi:[1,0]
	v_rcp_f32_e32 v231, v221
	v_fmamk_f32 v117, v121, 0x41000000, v252
	v_fmamk_f32 v121, v197, 0x41000000, v252
	v_pk_mul_f32 v[114:115], v[114:115], v[220:221] op_sel_hi:[1,0]
	v_pk_mul_f32 v[112:113], v[112:113], v[220:221] op_sel_hi:[1,0]
	v_rcp_f32_e32 v221, v121
	v_exp_f32_e32 v121, v118
	v_exp_f32_e32 v197, v119
	v_rcp_f32_e32 v230, v207
	v_lshlrev_b32_e32 v212, 16, v213
	v_and_b32_e32 v213, 0xffff0000, v213
	v_fmamk_f32 v119, v121, 0x41000000, v252
	v_fmamk_f32 v121, v197, 0x41000000, v252
	v_pk_fma_f32 v[132:133], v[230:231], v[132:133], v[212:213]
	v_rcp_f32_e32 v231, v121
	v_exp_f32_e32 v121, v112
	v_exp_f32_e32 v197, v113
	v_exp_f32_e32 v114, v114
	v_exp_f32_e32 v115, v115
	v_lshlrev_b32_e32 v212, 16, v214
	v_and_b32_e32 v213, 0xffff0000, v214
	v_lshlrev_b32_e32 v214, 16, v215
	v_and_b32_e32 v215, 0xffff0000, v215
	v_cvt_f32_fp8_e32 v116, v226
	v_rcp_f32_e32 v220, v117
	v_cvt_f32_fp8_sdwa v117, v226 src0_sel:BYTE_1
	v_pk_fma_f32 v[214:215], v[224:225], v[122:123], v[214:215]
	v_pk_mul_f32 v[122:123], v[134:135], v[134:135]
	v_cvt_f32_fp8_sdwa v118, v226 src0_sel:BYTE_2
	v_rcp_f32_e32 v230, v119
	v_cvt_f32_fp8_sdwa v119, v226 src0_sel:BYTE_3
	v_fmamk_f32 v113, v121, 0x41000000, v252
	v_fmamk_f32 v121, v197, 0x41000000, v252
	v_cvt_pk_bf16_f32 v120, v134, v135
	v_pk_mul_f32 v[134:135], v[132:133], v[132:133]
	v_cvt_f32_fp8_e32 v112, v227
	v_mov_b32_e32 v228, v232
	v_rcp_f32_e32 v232, v113
	v_cvt_f32_fp8_sdwa v113, v227 src0_sel:BYTE_1
	v_mov_b32_e32 v229, v233
	v_rcp_f32_e32 v233, v121
	v_fmamk_f32 v114, v114, 0x41000000, v252
	v_add_f32_e32 v121, v122, v123
	v_pk_fma_f32 v[212:213], v[244:245], v[228:229], v[212:213]
	v_cvt_f32_fp8_sdwa v226, v227 src0_sel:BYTE_2
	v_rcp_f32_e32 v244, v114
	v_cvt_f32_fp8_sdwa v227, v227 src0_sel:BYTE_3
	v_fmamk_f32 v114, v115, 0x41000000, v252
	v_add_f32_e32 v121, v134, v121
	v_pk_mul_f32 v[224:225], v[212:213], v[212:213]
	v_rcp_f32_e32 v245, v114
	v_lshlrev_b32_e32 v114, 16, v216
	v_and_b32_e32 v115, 0xffff0000, v216
	v_add_f32_e32 v121, v135, v121
	v_pk_fma_f32 v[220:221], v[220:221], v[116:117], v[114:115]
	v_lshlrev_b32_e32 v114, 16, v217
	v_and_b32_e32 v115, 0xffff0000, v217
	v_add_f32_e32 v121, v224, v121
	v_pk_mul_f32 v[228:229], v[214:215], v[214:215]
	v_pk_fma_f32 v[114:115], v[230:231], v[118:119], v[114:115]
	v_lshlrev_b32_e32 v116, 16, v218
	v_and_b32_e32 v117, 0xffff0000, v218
	v_add_f32_e32 v121, v225, v121
	v_pk_fma_f32 v[116:117], v[232:233], v[112:113], v[116:117]
	v_lshlrev_b32_e32 v112, 16, v219
	v_and_b32_e32 v113, 0xffff0000, v219
	v_add_f32_e32 v121, v228, v121
	v_pk_fma_f32 v[118:119], v[244:245], v[226:227], v[112:113]
	v_pk_mul_f32 v[112:113], v[220:221], v[220:221]
	v_add_f32_e32 v121, v229, v121
	v_add_f32_e32 v112, v121, v112
	v_pk_mul_f32 v[216:217], v[114:115], v[114:115]
	v_add_f32_e32 v112, v113, v112
	v_add_f32_e32 v112, v216, v112
	v_pk_mul_f32 v[218:219], v[116:117], v[116:117]
	v_add_f32_e32 v112, v217, v112
	v_add_f32_e32 v112, v218, v112
	v_pk_mul_f32 v[226:227], v[118:119], v[118:119]
	v_add_f32_e32 v112, v219, v112
	v_add_f32_e32 v112, v226, v112
	v_add_f32_e32 v113, v227, v112
	ds_bpermute_b32 v134, v242, v113
	v_mul_f32_e32 v206, 0xbfb8aa3b, v206
	v_pk_mul_f32 v[108:109], v[108:109], v[206:207] op_sel_hi:[1,0]
	v_cvt_pk_bf16_f32 v121, v132, v133
	s_waitcnt lgkmcnt(0)
	v_add_f32_e32 v197, v113, v134
	v_exp_f32_e32 v113, v108
	v_exp_f32_e32 v133, v109
	v_pk_mul_f32 v[110:111], v[110:111], v[206:207] op_sel_hi:[1,0]
	v_pk_mul_f32 v[104:105], v[104:105], v[206:207] op_sel_hi:[1,0]
	v_fmamk_f32 v109, v113, 0x41000000, v252
	v_fmamk_f32 v113, v133, 0x41000000, v252
	v_rcp_f32_e32 v133, v113
	v_exp_f32_e32 v113, v110
	v_exp_f32_e32 v135, v111
	v_fmamk_f32 v111, v113, 0x41000000, v252
	v_fmamk_f32 v113, v135, 0x41000000, v252
	v_rcp_f32_e32 v135, v113
	v_exp_f32_e32 v113, v104
	v_exp_f32_e32 v203, v105
	v_pk_mul_f32 v[106:107], v[106:107], v[206:207] op_sel_hi:[1,0]
	v_cvt_pk_bf16_f32 v122, v212, v213
	v_fmamk_f32 v105, v113, 0x41000000, v252
	v_fmamk_f32 v113, v203, 0x41000000, v252
	v_rcp_f32_e32 v213, v113
	v_exp_f32_e32 v113, v106
	v_exp_f32_e32 v203, v107
	v_pk_mul_f32 v[100:101], v[100:101], v[206:207] op_sel_hi:[1,0]
	v_cvt_f32_fp8_e32 v108, v210
	v_fmamk_f32 v107, v113, 0x41000000, v252
	v_fmamk_f32 v113, v203, 0x41000000, v252
	v_rcp_f32_e32 v132, v109
	v_cvt_f32_fp8_sdwa v109, v210 src0_sel:BYTE_1
	v_cvt_f32_fp8_sdwa v110, v210 src0_sel:BYTE_2
	v_rcp_f32_e32 v134, v111
	v_cvt_f32_fp8_sdwa v111, v210 src0_sel:BYTE_3
	v_cvt_f32_fp8_e32 v104, v211
	v_rcp_f32_e32 v212, v105
	v_cvt_f32_fp8_sdwa v105, v211 src0_sel:BYTE_1
	v_cvt_f32_fp8_sdwa v106, v211 src0_sel:BYTE_2
	v_rcp_f32_e32 v210, v107
	v_cvt_f32_fp8_sdwa v107, v211 src0_sel:BYTE_3
	v_rcp_f32_e32 v211, v113
	v_exp_f32_e32 v113, v100
	v_exp_f32_e32 v203, v101
	v_pk_mul_f32 v[102:103], v[102:103], v[206:207] op_sel_hi:[1,0]
	v_pk_mul_f32 v[98:99], v[98:99], v[206:207] op_sel_hi:[1,0]
	v_fmamk_f32 v101, v113, 0x41000000, v252
	v_fmamk_f32 v113, v203, 0x41000000, v252
	v_pk_mul_f32 v[96:97], v[96:97], v[206:207] op_sel_hi:[1,0]
	v_rcp_f32_e32 v207, v113
	v_exp_f32_e32 v113, v102
	v_exp_f32_e32 v203, v103
	v_cvt_pk_bf16_f32 v123, v214, v215
	v_lshlrev_b32_e32 v214, 16, v148
	v_and_b32_e32 v215, 0xffff0000, v148
	v_pk_fma_f32 v[132:133], v[132:133], v[108:109], v[214:215]
	v_lshlrev_b32_e32 v108, 16, v149
	v_and_b32_e32 v109, 0xffff0000, v149
	v_pk_fma_f32 v[134:135], v[134:135], v[110:111], v[108:109]
	v_lshlrev_b32_e32 v108, 16, v150
	v_and_b32_e32 v109, 0xffff0000, v150
	v_pk_fma_f32 v[148:149], v[212:213], v[104:105], v[108:109]
	v_lshlrev_b32_e32 v104, 16, v151
	v_and_b32_e32 v105, 0xffff0000, v151
	v_fmamk_f32 v103, v113, 0x41000000, v252
	v_fmamk_f32 v113, v203, 0x41000000, v252
	v_pk_fma_f32 v[150:151], v[210:211], v[106:107], v[104:105]
	v_rcp_f32_e32 v211, v113
	v_exp_f32_e32 v113, v96
	v_exp_f32_e32 v203, v97
	v_fmamk_f32 v97, v113, 0x41000000, v252
	v_fmamk_f32 v113, v203, 0x41000000, v252
	v_rcp_f32_e32 v213, v113
	v_exp_f32_e32 v113, v98
	v_exp_f32_e32 v203, v99
	v_cvt_f32_fp8_e32 v100, v204
	v_rcp_f32_e32 v206, v101
	v_cvt_f32_fp8_sdwa v101, v204 src0_sel:BYTE_1
	v_pk_mul_f32 v[104:105], v[132:133], v[132:133]
	v_cvt_f32_fp8_sdwa v102, v204 src0_sel:BYTE_2
	v_rcp_f32_e32 v210, v103
	v_cvt_f32_fp8_sdwa v103, v204 src0_sel:BYTE_3
	v_pk_mul_f32 v[106:107], v[134:135], v[134:135]
	v_cvt_f32_fp8_e32 v96, v205
	v_rcp_f32_e32 v212, v97
	v_cvt_f32_fp8_sdwa v97, v205 src0_sel:BYTE_1
	v_fmamk_f32 v99, v113, 0x41000000, v252
	v_add_f32_e32 v104, v104, v105
	v_cvt_f32_fp8_sdwa v98, v205 src0_sel:BYTE_2
	v_rcp_f32_e32 v214, v99
	v_cvt_f32_fp8_sdwa v99, v205 src0_sel:BYTE_3
	v_fmamk_f32 v113, v203, 0x41000000, v252
	v_add_f32_e32 v104, v106, v104
	v_pk_mul_f32 v[108:109], v[148:149], v[148:149]
	v_rcp_f32_e32 v215, v113
	v_lshlrev_b32_e32 v204, 16, v144
	v_and_b32_e32 v205, 0xffff0000, v144
	v_add_f32_e32 v104, v107, v104
	v_pk_fma_f32 v[204:205], v[206:207], v[100:101], v[204:205]
	v_lshlrev_b32_e32 v100, 16, v145
	v_and_b32_e32 v101, 0xffff0000, v145
	v_add_f32_e32 v104, v108, v104
	v_pk_mul_f32 v[110:111], v[150:151], v[150:151]
	v_pk_fma_f32 v[144:145], v[210:211], v[102:103], v[100:101]
	v_lshlrev_b32_e32 v100, 16, v146
	v_and_b32_e32 v101, 0xffff0000, v146
	v_add_f32_e32 v104, v109, v104
	v_pk_fma_f32 v[206:207], v[212:213], v[96:97], v[100:101]
	v_lshlrev_b32_e32 v96, 16, v147
	v_and_b32_e32 v97, 0xffff0000, v147
	v_add_f32_e32 v104, v110, v104
	v_pk_fma_f32 v[146:147], v[214:215], v[98:99], v[96:97]
	v_pk_mul_f32 v[96:97], v[204:205], v[204:205]
	v_add_f32_e32 v104, v111, v104
	v_add_f32_e32 v96, v104, v96
	v_pk_mul_f32 v[98:99], v[144:145], v[144:145]
	v_add_f32_e32 v96, v97, v96
	v_add_f32_e32 v96, v98, v96
	v_pk_mul_f32 v[100:101], v[206:207], v[206:207]
	v_add_f32_e32 v96, v99, v96
	v_add_f32_e32 v96, v100, v96
	v_pk_mul_f32 v[102:103], v[146:147], v[146:147]
	v_add_f32_e32 v96, v101, v96
	v_mul_f32_e32 v202, 0xbfb8aa3b, v202
	v_pk_mul_f32 v[92:93], v[92:93], v[202:203] op_sel_hi:[1,0]
	v_add_f32_e32 v96, v102, v96
	v_pk_mul_f32 v[94:95], v[94:95], v[202:203] op_sel_hi:[1,0]
	v_add_f32_e32 v106, v103, v96
	v_pk_mul_f32 v[88:89], v[88:89], v[202:203] op_sel_hi:[1,0]
	v_exp_f32_e32 v96, v92
	v_pk_mul_f32 v[90:91], v[90:91], v[202:203] op_sel_hi:[1,0]
	v_exp_f32_e32 v97, v93
	v_exp_f32_e32 v98, v94
	v_exp_f32_e32 v99, v95
	v_exp_f32_e32 v100, v88
	v_exp_f32_e32 v101, v89
	v_exp_f32_e32 v102, v90
	v_fmamk_f32 v93, v96, 0x41000000, v252
	v_exp_f32_e32 v103, v91
	v_cvt_f32_fp8_e32 v92, v208
	v_rcp_f32_e32 v96, v93
	v_cvt_f32_fp8_sdwa v93, v208 src0_sel:BYTE_1
	v_fmamk_f32 v97, v97, 0x41000000, v252
	v_fmamk_f32 v95, v98, 0x41000000, v252
	v_rcp_f32_e32 v97, v97
	v_cvt_f32_fp8_sdwa v94, v208 src0_sel:BYTE_2
	v_rcp_f32_e32 v98, v95
	v_cvt_f32_fp8_sdwa v95, v208 src0_sel:BYTE_3
	v_fmamk_f32 v99, v99, 0x41000000, v252
	v_fmamk_f32 v89, v100, 0x41000000, v252
	v_rcp_f32_e32 v99, v99
	v_cvt_f32_fp8_e32 v88, v209
	v_rcp_f32_e32 v100, v89
	v_cvt_f32_fp8_sdwa v89, v209 src0_sel:BYTE_1
	v_fmamk_f32 v101, v101, 0x41000000, v252
	v_fmamk_f32 v91, v102, 0x41000000, v252
	v_rcp_f32_e32 v101, v101
	v_cvt_f32_fp8_sdwa v90, v209 src0_sel:BYTE_2
	v_rcp_f32_e32 v102, v91
	v_cvt_f32_fp8_sdwa v91, v209 src0_sel:BYTE_3
	v_fmamk_f32 v103, v103, 0x41000000, v252
	v_pk_mul_f32 v[84:85], v[84:85], v[202:203] op_sel_hi:[1,0]
	v_rcp_f32_e32 v103, v103
	v_lshlrev_b32_e32 v104, 16, v140
	v_and_b32_e32 v105, 0xffff0000, v140
	v_pk_mul_f32 v[86:87], v[86:87], v[202:203] op_sel_hi:[1,0]
	v_pk_fma_f32 v[208:209], v[96:97], v[92:93], v[104:105]
	v_lshlrev_b32_e32 v92, 16, v141
	v_and_b32_e32 v93, 0xffff0000, v141
	v_pk_mul_f32 v[80:81], v[80:81], v[202:203] op_sel_hi:[1,0]
	v_exp_f32_e32 v96, v84
	v_pk_fma_f32 v[140:141], v[98:99], v[94:95], v[92:93]
	v_lshlrev_b32_e32 v92, 16, v142
	v_and_b32_e32 v93, 0xffff0000, v142
	v_pk_mul_f32 v[82:83], v[82:83], v[202:203] op_sel_hi:[1,0]
	v_exp_f32_e32 v97, v85
	v_exp_f32_e32 v98, v86
	v_pk_fma_f32 v[210:211], v[100:101], v[88:89], v[92:93]
	v_lshlrev_b32_e32 v88, 16, v143
	v_and_b32_e32 v89, 0xffff0000, v143
	v_exp_f32_e32 v99, v87
	v_exp_f32_e32 v100, v80
	v_pk_fma_f32 v[142:143], v[102:103], v[90:91], v[88:89]
	v_exp_f32_e32 v101, v81
	v_exp_f32_e32 v102, v82
	v_fmamk_f32 v85, v96, 0x41000000, v252
	v_exp_f32_e32 v103, v83
	v_cvt_f32_fp8_e32 v84, v200
	v_rcp_f32_e32 v96, v85
	v_cvt_f32_fp8_sdwa v85, v200 src0_sel:BYTE_1
	v_fmamk_f32 v97, v97, 0x41000000, v252
	v_fmamk_f32 v87, v98, 0x41000000, v252
	v_pk_mul_f32 v[88:89], v[208:209], v[208:209]
	v_rcp_f32_e32 v97, v97
	v_cvt_f32_fp8_sdwa v86, v200 src0_sel:BYTE_2
	v_rcp_f32_e32 v98, v87
	v_cvt_f32_fp8_sdwa v87, v200 src0_sel:BYTE_3
	v_fmamk_f32 v99, v99, 0x41000000, v252
	v_fmamk_f32 v81, v100, 0x41000000, v252
	v_pk_mul_f32 v[90:91], v[140:141], v[140:141]
	v_rcp_f32_e32 v99, v99
	v_cvt_f32_fp8_e32 v80, v201
	v_rcp_f32_e32 v100, v81
	v_cvt_f32_fp8_sdwa v81, v201 src0_sel:BYTE_1
	v_fmamk_f32 v101, v101, 0x41000000, v252
	v_fmamk_f32 v83, v102, 0x41000000, v252
	v_add_f32_e32 v88, v88, v89
	v_rcp_f32_e32 v101, v101
	v_cvt_f32_fp8_sdwa v82, v201 src0_sel:BYTE_2
	v_rcp_f32_e32 v102, v83
	v_cvt_f32_fp8_sdwa v83, v201 src0_sel:BYTE_3
	v_fmamk_f32 v103, v103, 0x41000000, v252
	v_add_f32_e32 v88, v90, v88
	v_pk_mul_f32 v[92:93], v[210:211], v[210:211]
	v_rcp_f32_e32 v103, v103
	v_lshlrev_b32_e32 v104, 16, v136
	v_and_b32_e32 v105, 0xffff0000, v136
	v_add_f32_e32 v88, v91, v88
	v_pk_fma_f32 v[200:201], v[96:97], v[84:85], v[104:105]
	v_lshlrev_b32_e32 v84, 16, v137
	v_and_b32_e32 v85, 0xffff0000, v137
	v_add_f32_e32 v88, v92, v88
	v_pk_mul_f32 v[94:95], v[142:143], v[142:143]
	v_pk_fma_f32 v[202:203], v[98:99], v[86:87], v[84:85]
	v_lshlrev_b32_e32 v84, 16, v138
	v_and_b32_e32 v85, 0xffff0000, v138
	v_add_f32_e32 v88, v93, v88
	v_pk_fma_f32 v[212:213], v[100:101], v[80:81], v[84:85]
	v_lshlrev_b32_e32 v80, 16, v139
	v_and_b32_e32 v81, 0xffff0000, v139
	v_add_f32_e32 v88, v94, v88
	v_pk_fma_f32 v[214:215], v[102:103], v[82:83], v[80:81]
	v_pk_mul_f32 v[80:81], v[200:201], v[200:201]
	v_add_f32_e32 v88, v95, v88
	v_add_f32_e32 v80, v88, v80
	v_pk_mul_f32 v[82:83], v[202:203], v[202:203]
	v_add_f32_e32 v80, v81, v80
	v_add_f32_e32 v80, v82, v80
	v_pk_mul_f32 v[84:85], v[212:213], v[212:213]
	v_add_f32_e32 v80, v83, v80
	v_add_f32_e32 v80, v84, v80
	v_pk_mul_f32 v[86:87], v[214:215], v[214:215]
	v_add_f32_e32 v80, v85, v80
	v_mul_f32_e32 v196, 0xbfb8aa3b, v196
	v_pk_mul_f32 v[76:77], v[76:77], v[196:197] op_sel_hi:[1,0]
	v_add_f32_e32 v80, v86, v80
	v_pk_mul_f32 v[78:79], v[78:79], v[196:197] op_sel_hi:[1,0]
	v_add_f32_e32 v90, v87, v80
	v_pk_mul_f32 v[72:73], v[72:73], v[196:197] op_sel_hi:[1,0]
	v_exp_f32_e32 v80, v76
	v_pk_mul_f32 v[74:75], v[74:75], v[196:197] op_sel_hi:[1,0]
	v_exp_f32_e32 v81, v77
	v_exp_f32_e32 v82, v78
	v_exp_f32_e32 v83, v79
	v_exp_f32_e32 v84, v72
	v_exp_f32_e32 v85, v73
	v_exp_f32_e32 v86, v74
	v_fmamk_f32 v77, v80, 0x41000000, v252
	v_exp_f32_e32 v87, v75
	v_cvt_f32_fp8_e32 v76, v198
	v_rcp_f32_e32 v80, v77
	v_cvt_f32_fp8_sdwa v77, v198 src0_sel:BYTE_1
	v_fmamk_f32 v81, v81, 0x41000000, v252
	v_fmamk_f32 v79, v82, 0x41000000, v252
	v_rcp_f32_e32 v81, v81
	v_cvt_f32_fp8_sdwa v78, v198 src0_sel:BYTE_2
	v_rcp_f32_e32 v82, v79
	v_cvt_f32_fp8_sdwa v79, v198 src0_sel:BYTE_3
	v_fmamk_f32 v83, v83, 0x41000000, v252
	v_fmamk_f32 v73, v84, 0x41000000, v252
	v_rcp_f32_e32 v83, v83
	v_cvt_f32_fp8_e32 v72, v199
	v_rcp_f32_e32 v84, v73
	v_cvt_f32_fp8_sdwa v73, v199 src0_sel:BYTE_1
	v_fmamk_f32 v85, v85, 0x41000000, v252
	v_fmamk_f32 v75, v86, 0x41000000, v252
	v_rcp_f32_e32 v85, v85
	v_cvt_f32_fp8_sdwa v74, v199 src0_sel:BYTE_2
	v_rcp_f32_e32 v86, v75
	v_cvt_f32_fp8_sdwa v75, v199 src0_sel:BYTE_3
	v_fmamk_f32 v87, v87, 0x41000000, v252
	v_pk_mul_f32 v[68:69], v[68:69], v[196:197] op_sel_hi:[1,0]
	v_rcp_f32_e32 v87, v87
	v_lshlrev_b32_e32 v88, 16, v128
	v_and_b32_e32 v89, 0xffff0000, v128
	v_pk_mul_f32 v[70:71], v[70:71], v[196:197] op_sel_hi:[1,0]
	v_pk_fma_f32 v[198:199], v[80:81], v[76:77], v[88:89]
	v_lshlrev_b32_e32 v76, 16, v129
	v_and_b32_e32 v77, 0xffff0000, v129
	v_pk_mul_f32 v[64:65], v[64:65], v[196:197] op_sel_hi:[1,0]
	v_exp_f32_e32 v80, v68
	v_pk_fma_f32 v[216:217], v[82:83], v[78:79], v[76:77]
	v_lshlrev_b32_e32 v76, 16, v130
	v_and_b32_e32 v77, 0xffff0000, v130
	v_pk_mul_f32 v[66:67], v[66:67], v[196:197] op_sel_hi:[1,0]
	v_exp_f32_e32 v81, v69
	v_exp_f32_e32 v82, v70
	v_pk_fma_f32 v[218:219], v[84:85], v[72:73], v[76:77]
	v_lshlrev_b32_e32 v72, 16, v131
	v_and_b32_e32 v73, 0xffff0000, v131
	v_exp_f32_e32 v83, v71
	v_exp_f32_e32 v84, v64
	v_cvt_pk_bf16_f32 v112, v220, v221
	v_pk_fma_f32 v[220:221], v[86:87], v[74:75], v[72:73]
	v_exp_f32_e32 v85, v65
	v_exp_f32_e32 v86, v66
	v_fmamk_f32 v69, v80, 0x41000000, v252
	v_exp_f32_e32 v87, v67
	v_cvt_f32_fp8_e32 v68, v194
	v_rcp_f32_e32 v80, v69
	v_cvt_f32_fp8_sdwa v69, v194 src0_sel:BYTE_1
	v_fmamk_f32 v81, v81, 0x41000000, v252
	v_fmamk_f32 v71, v82, 0x41000000, v252
	v_pk_mul_f32 v[72:73], v[198:199], v[198:199]
	v_rcp_f32_e32 v81, v81
	v_cvt_f32_fp8_sdwa v70, v194 src0_sel:BYTE_2
	v_rcp_f32_e32 v82, v71
	v_cvt_f32_fp8_sdwa v71, v194 src0_sel:BYTE_3
	v_fmamk_f32 v83, v83, 0x41000000, v252
	v_fmamk_f32 v65, v84, 0x41000000, v252
	v_pk_mul_f32 v[74:75], v[216:217], v[216:217]
	v_rcp_f32_e32 v83, v83
	v_cvt_f32_fp8_e32 v64, v195
	v_rcp_f32_e32 v84, v65
	v_cvt_f32_fp8_sdwa v65, v195 src0_sel:BYTE_1
	v_fmamk_f32 v85, v85, 0x41000000, v252
	v_fmamk_f32 v67, v86, 0x41000000, v252
	v_add_f32_e32 v72, v72, v73
	v_rcp_f32_e32 v85, v85
	v_cvt_f32_fp8_sdwa v66, v195 src0_sel:BYTE_2
	v_rcp_f32_e32 v86, v67
	v_cvt_f32_fp8_sdwa v67, v195 src0_sel:BYTE_3
	v_fmamk_f32 v87, v87, 0x41000000, v252
	v_add_f32_e32 v72, v74, v72
	v_pk_mul_f32 v[76:77], v[218:219], v[218:219]
	v_rcp_f32_e32 v87, v87
	v_lshlrev_b32_e32 v88, 16, v124
	v_and_b32_e32 v89, 0xffff0000, v124
	v_add_f32_e32 v72, v75, v72
	v_pk_fma_f32 v[226:227], v[80:81], v[68:69], v[88:89]
	v_lshlrev_b32_e32 v68, 16, v125
	v_and_b32_e32 v69, 0xffff0000, v125
	v_add_f32_e32 v72, v76, v72
	v_pk_mul_f32 v[78:79], v[220:221], v[220:221]
	v_pk_fma_f32 v[228:229], v[82:83], v[70:71], v[68:69]
	v_lshlrev_b32_e32 v68, 16, v126
	v_and_b32_e32 v69, 0xffff0000, v126
	v_add_f32_e32 v72, v77, v72
	v_pk_fma_f32 v[230:231], v[84:85], v[64:65], v[68:69]
	v_lshlrev_b32_e32 v64, 16, v127
	v_and_b32_e32 v65, 0xffff0000, v127
	v_add_f32_e32 v72, v78, v72
	v_pk_fma_f32 v[232:233], v[86:87], v[66:67], v[64:65]
	v_pk_mul_f32 v[64:65], v[226:227], v[226:227]
	v_add_f32_e32 v72, v79, v72
	v_add_f32_e32 v64, v72, v64
	v_pk_mul_f32 v[66:67], v[228:229], v[228:229]
	v_add_f32_e32 v64, v65, v64
	v_add_f32_e32 v64, v66, v64
	v_pk_mul_f32 v[68:69], v[230:231], v[230:231]
	v_add_f32_e32 v64, v67, v64
	v_add_f32_e32 v64, v68, v64
	v_pk_mul_f32 v[70:71], v[232:233], v[232:233]
	v_add_f32_e32 v64, v69, v64
	v_add_f32_e32 v64, v70, v64
	v_add_f32_e32 v64, v71, v64
	ds_bpermute_b32 v107, v242, v106
	ds_bpermute_b32 v91, v242, v90
	ds_bpermute_b32 v65, v242, v64
	ds_bpermute_b32 v222, v241, v197
	v_cvt_pk_bf16_f32 v113, v114, v115
	s_waitcnt lgkmcnt(3)
	v_add_f32_e32 v245, v106, v107
	s_waitcnt lgkmcnt(2)
	v_add_f32_e32 v243, v90, v91
	s_waitcnt lgkmcnt(1)
	v_add_f32_e32 v129, v64, v65
	ds_bpermute_b32 v246, v241, v245
	ds_bpermute_b32 v244, v241, v243
	ds_bpermute_b32 v139, v241, v129
	v_cvt_pk_bf16_f32 v115, v118, v119
	s_waitcnt lgkmcnt(3)
	v_add_f32_e32 v119, v197, v222
	v_cvt_pk_bf16_f32 v114, v116, v117
	v_add_u32_e32 v108, 0x80, v172
	v_ashrrev_i32_e32 v109, 31, v108
	v_lshlrev_b64 v[64:65], 10, v[108:109]
	v_lshlrev_b64 v[110:111], 11, v[108:109]
	v_add_u32_e32 v104, 0x90, v172
	v_lshl_add_u64 v[66:67], v[192:193], 0, v[110:111]
	v_lshl_add_u64 v[64:65], v[178:179], 0, v[64:65]
	v_ashrrev_i32_e32 v105, 31, v104
	global_load_dwordx4 v[92:95], v[66:67], off nt
	global_load_dwordx4 v[88:91], v[66:67], off offset:256 nt
	global_load_dwordx2 v[224:225], v[64:65], off nt
	global_load_dwordx2 v[196:197], v[64:65], off offset:128 nt
	v_lshlrev_b64 v[64:65], 10, v[104:105]
	v_lshlrev_b64 v[106:107], 11, v[104:105]
	v_add_u32_e32 v98, 0xa0, v172
	v_lshl_add_u64 v[66:67], v[192:193], 0, v[106:107]
	v_lshl_add_u64 v[64:65], v[178:179], 0, v[64:65]
	v_ashrrev_i32_e32 v99, 31, v98
	global_load_dwordx4 v[84:87], v[66:67], off nt
	global_load_dwordx4 v[80:83], v[66:67], off offset:256 nt
	global_load_dwordx2 v[194:195], v[64:65], off nt
	global_load_dwordx2 v[136:137], v[64:65], off offset:128 nt
	v_lshlrev_b64 v[64:65], 10, v[98:99]
	v_lshlrev_b64 v[102:103], 11, v[98:99]
	v_add_u32_e32 v96, 0xb0, v172
	v_lshl_add_u64 v[66:67], v[192:193], 0, v[102:103]
	v_lshl_add_u64 v[64:65], v[178:179], 0, v[64:65]
	v_ashrrev_i32_e32 v97, 31, v96
	global_load_dwordx4 v[76:79], v[66:67], off nt
	global_load_dwordx4 v[72:75], v[66:67], off offset:256 nt
	global_load_dwordx2 v[130:131], v[64:65], off nt
	global_load_dwordx2 v[126:127], v[64:65], off offset:128 nt
	v_lshlrev_b64 v[64:65], 10, v[96:97]
	v_lshlrev_b64 v[100:101], 11, v[96:97]
	v_lshl_add_u64 v[66:67], v[192:193], 0, v[100:101]
	v_lshl_add_u64 v[116:117], v[178:179], 0, v[64:65]
	global_load_dword v222, v[180:181], off offset:512
	global_load_dword v138, v[180:181], off offset:576
	global_load_dword v128, v[180:181], off offset:640
	global_load_dword v118, v[180:181], off offset:704
	global_load_dwordx4 v[68:71], v[66:67], off nt
	s_nop 0
	global_load_dwordx4 v[64:67], v[66:67], off offset:256 nt
	s_nop 0
	global_load_dwordx2 v[124:125], v[116:117], off nt
	s_nop 0
	global_load_dwordx2 v[116:117], v[116:117], off offset:128 nt
	v_lshl_add_u64 v[178:179], s[40:41], 0, v[190:191]
	v_lshl_add_u64 v[178:179], v[178:179], 0, v[188:189]
	global_store_dwordx4 v[178:179], v[120:123], off
	global_store_dwordx4 v[178:179], v[112:115], off offset:256
	s_and_saveexec_b64 s[20:21], s[2:3]
	s_cbranch_execz .LBB0_1094
	v_lshl_add_u64 v[112:113], v[172:173], 2, s[0:1]
	global_atomic_add_f32 v[112:113], v119, off

.LBB0_1100:
	s_or_b64 exec, exec, s[20:21]
	s_waitcnt vmcnt(15)
	v_mul_f32_e32 v222, 0xbfb8aa3b, v222
	v_pk_mul_f32 v[62:63], v[62:63], v[222:223] op_sel_hi:[1,0]
	v_pk_mul_f32 v[56:57], v[56:57], v[222:223] op_sel_hi:[1,0]
	v_exp_f32_e32 v114, v62
	v_exp_f32_e32 v115, v63
	v_exp_f32_e32 v119, v56
	v_exp_f32_e32 v121, v57
	v_pk_mul_f32 v[58:59], v[58:59], v[222:223] op_sel_hi:[1,0]
	v_fmamk_f32 v63, v114, 0x41000000, v252
	v_cvt_f32_fp8_sdwa v62, v224 src0_sel:BYTE_2
	v_rcp_f32_e32 v114, v63
	v_cvt_f32_fp8_sdwa v63, v224 src0_sel:BYTE_3
	v_fmamk_f32 v115, v115, 0x41000000, v252
	v_fmamk_f32 v57, v119, 0x41000000, v252
	v_fmamk_f32 v119, v121, 0x41000000, v252
	v_rcp_f32_e32 v115, v115
	v_cvt_f32_fp8_e32 v56, v225
	v_rcp_f32_e32 v120, v57
	v_cvt_f32_fp8_sdwa v57, v225 src0_sel:BYTE_1
	v_rcp_f32_e32 v121, v119
	v_exp_f32_e32 v119, v58
	v_exp_f32_e32 v123, v59
	v_lshlrev_b32_e32 v132, 16, v92
	v_and_b32_e32 v133, 0xffff0000, v92
	v_lshlrev_b32_e32 v92, 16, v93
	v_and_b32_e32 v93, 0xffff0000, v93
	v_pk_mul_f32 v[52:53], v[52:53], v[222:223] op_sel_hi:[1,0]
	v_fmamk_f32 v59, v119, 0x41000000, v252
	v_fmamk_f32 v119, v123, 0x41000000, v252
	v_pk_fma_f32 v[62:63], v[114:115], v[62:63], v[92:93]
	v_lshlrev_b32_e32 v92, 16, v94
	v_and_b32_e32 v93, 0xffff0000, v94
	v_cvt_f32_fp8_sdwa v58, v225 src0_sel:BYTE_2
	v_rcp_f32_e32 v122, v59
	v_cvt_f32_fp8_sdwa v59, v225 src0_sel:BYTE_3
	v_rcp_f32_e32 v123, v119
	v_pk_fma_f32 v[56:57], v[120:121], v[56:57], v[92:93]
	v_exp_f32_e32 v119, v52
	v_exp_f32_e32 v121, v53
	v_pk_mul_f32 v[60:61], v[60:61], v[222:223] op_sel_hi:[1,0]
	v_pk_mul_f32 v[54:55], v[54:55], v[222:223] op_sel_hi:[1,0]
	v_lshlrev_b32_e32 v92, 16, v95
	v_and_b32_e32 v93, 0xffff0000, v95
	v_fmamk_f32 v53, v119, 0x41000000, v252
	v_fmamk_f32 v119, v121, 0x41000000, v252
	v_exp_f32_e32 v112, v60
	v_pk_fma_f32 v[58:59], v[122:123], v[58:59], v[92:93]
	v_rcp_f32_e32 v121, v119
	v_exp_f32_e32 v119, v54
	v_exp_f32_e32 v123, v55
	v_exp_f32_e32 v113, v61
	v_pk_mul_f32 v[48:49], v[48:49], v[222:223] op_sel_hi:[1,0]
	v_fmamk_f32 v61, v112, 0x41000000, v252
	v_fmamk_f32 v55, v119, 0x41000000, v252
	v_fmamk_f32 v119, v123, 0x41000000, v252
	v_cvt_f32_fp8_e32 v60, v224
	v_rcp_f32_e32 v112, v61
	v_cvt_f32_fp8_sdwa v61, v224 src0_sel:BYTE_1
	v_fmamk_f32 v113, v113, 0x41000000, v252
	v_rcp_f32_e32 v123, v119
	v_exp_f32_e32 v119, v48
	v_exp_f32_e32 v129, v49
	v_rcp_f32_e32 v113, v113
	v_pk_mul_f32 v[50:51], v[50:51], v[222:223] op_sel_hi:[1,0]
	v_fmamk_f32 v49, v119, 0x41000000, v252
	v_fmamk_f32 v119, v129, 0x41000000, v252
	v_pk_fma_f32 v[60:61], v[112:113], v[60:61], v[132:133]
	v_rcp_f32_e32 v133, v119
	v_exp_f32_e32 v119, v50
	v_exp_f32_e32 v129, v51
	v_pk_mul_f32 v[92:93], v[60:61], v[60:61]
	v_cvt_f32_fp8_sdwa v54, v196 src0_sel:BYTE_2
	v_rcp_f32_e32 v122, v55
	v_cvt_f32_fp8_sdwa v55, v196 src0_sel:BYTE_3
	v_pk_mul_f32 v[94:95], v[62:63], v[62:63]
	v_cvt_f32_fp8_e32 v52, v196
	v_rcp_f32_e32 v120, v53
	v_cvt_f32_fp8_sdwa v53, v196 src0_sel:BYTE_1
	v_cvt_f32_fp8_e32 v48, v197
	v_rcp_f32_e32 v132, v49
	v_cvt_f32_fp8_sdwa v49, v197 src0_sel:BYTE_1
	v_fmamk_f32 v51, v119, 0x41000000, v252
	v_add_f32_e32 v92, v92, v93
	v_cvt_f32_fp8_sdwa v50, v197 src0_sel:BYTE_2
	v_rcp_f32_e32 v134, v51
	v_cvt_f32_fp8_sdwa v51, v197 src0_sel:BYTE_3
	v_fmamk_f32 v119, v129, 0x41000000, v252
	v_add_f32_e32 v92, v94, v92
	v_pk_mul_f32 v[112:113], v[56:57], v[56:57]
	v_rcp_f32_e32 v135, v119
	v_add_f32_e32 v92, v95, v92
	v_lshlrev_b32_e32 v140, 16, v88
	v_and_b32_e32 v141, 0xffff0000, v88
	v_lshlrev_b32_e32 v88, 16, v89
	v_and_b32_e32 v89, 0xffff0000, v89
	v_add_f32_e32 v92, v112, v92
	v_pk_mul_f32 v[114:115], v[58:59], v[58:59]
	v_pk_fma_f32 v[54:55], v[122:123], v[54:55], v[88:89]
	v_lshlrev_b32_e32 v88, 16, v90
	v_and_b32_e32 v89, 0xffff0000, v90
	v_add_f32_e32 v92, v113, v92
	v_pk_fma_f32 v[52:53], v[120:121], v[52:53], v[140:141]
	v_pk_fma_f32 v[88:89], v[132:133], v[48:49], v[88:89]
	v_lshlrev_b32_e32 v48, 16, v91
	v_and_b32_e32 v49, 0xffff0000, v91
	v_add_f32_e32 v92, v114, v92
	v_pk_fma_f32 v[90:91], v[134:135], v[50:51], v[48:49]
	v_pk_mul_f32 v[48:49], v[52:53], v[52:53]
	v_add_f32_e32 v92, v115, v92
	v_add_f32_e32 v48, v92, v48
	v_pk_mul_f32 v[50:51], v[54:55], v[54:55]
	v_add_f32_e32 v48, v49, v48
	v_add_f32_e32 v48, v50, v48
	v_pk_mul_f32 v[120:121], v[88:89], v[88:89]
	v_add_f32_e32 v48, v51, v48
	v_add_f32_e32 v48, v120, v48
	v_pk_mul_f32 v[122:123], v[90:91], v[90:91]
	v_add_f32_e32 v48, v121, v48
	v_add_f32_e32 v48, v122, v48
	v_add_f32_e32 v92, v123, v48
	ds_bpermute_b32 v93, v242, v92
	v_cvt_pk_bf16_f32 v50, v56, v57
	s_waitcnt vmcnt(14)
	v_mul_f32_e32 v138, 0xbfb8aa3b, v138
	v_pk_mul_f32 v[44:45], v[44:45], v[138:139] op_sel_hi:[1,0]
	v_pk_mul_f32 v[40:41], v[40:41], v[138:139] op_sel_hi:[1,0]
	s_waitcnt lgkmcnt(0)
	v_add_f32_e32 v56, v92, v93
	ds_bpermute_b32 v57, v241, v56
	v_cvt_pk_bf16_f32 v51, v58, v59
	v_exp_f32_e32 v59, v45
	s_waitcnt lgkmcnt(0)
	v_add_f32_e32 v56, v56, v57
	v_exp_f32_e32 v57, v44
	v_exp_f32_e32 v40, v40
	v_exp_f32_e32 v41, v41
	v_pk_mul_f32 v[46:47], v[46:47], v[138:139] op_sel_hi:[1,0]
	v_fmamk_f32 v45, v57, 0x41000000, v252
	v_fmamk_f32 v57, v59, 0x41000000, v252
	v_fmamk_f32 v40, v40, 0x41000000, v252
	v_cvt_pk_bf16_f32 v52, v52, v53
	v_cvt_pk_bf16_f32 v53, v54, v55
	v_cvt_pk_bf16_f32 v54, v88, v89
	v_pk_mul_f32 v[42:43], v[42:43], v[138:139] op_sel_hi:[1,0]
	v_rcp_f32_e32 v59, v57
	v_exp_f32_e32 v57, v46
	v_rcp_f32_e32 v88, v40
	v_fmamk_f32 v40, v41, 0x41000000, v252
	v_cvt_pk_bf16_f32 v48, v60, v61
	v_exp_f32_e32 v61, v47
	v_rcp_f32_e32 v89, v40
	v_exp_f32_e32 v40, v42
	v_exp_f32_e32 v41, v43
	v_cvt_f32_fp8_e32 v44, v194
	v_rcp_f32_e32 v58, v45
	v_cvt_f32_fp8_sdwa v45, v194 src0_sel:BYTE_1
	v_fmamk_f32 v47, v57, 0x41000000, v252
	v_cvt_f32_fp8_sdwa v46, v194 src0_sel:BYTE_2
	v_rcp_f32_e32 v60, v47
	v_cvt_f32_fp8_sdwa v47, v194 src0_sel:BYTE_3
	v_fmamk_f32 v57, v61, 0x41000000, v252
	v_cvt_pk_bf16_f32 v49, v62, v63
	v_rcp_f32_e32 v61, v57
	v_cvt_f32_fp8_e32 v62, v195
	v_cvt_f32_fp8_sdwa v63, v195 src0_sel:BYTE_1
	v_fmamk_f32 v40, v40, 0x41000000, v252
	v_rcp_f32_e32 v92, v40
	v_fmamk_f32 v40, v41, 0x41000000, v252
	v_rcp_f32_e32 v93, v40
	v_lshlrev_b32_e32 v40, 16, v84
	v_and_b32_e32 v41, 0xffff0000, v84
	v_mov_b32_e32 v42, v44
	v_mov_b32_e32 v43, v45
	v_pk_fma_f32 v[40:41], v[58:59], v[42:43], v[40:41]
	v_lshlrev_b32_e32 v42, 16, v85
	v_and_b32_e32 v43, 0xffff0000, v85
	v_pk_mul_f32 v[36:37], v[36:37], v[138:139] op_sel_hi:[1,0]
	v_pk_mul_f32 v[32:33], v[32:33], v[138:139] op_sel_hi:[1,0]
	v_pk_fma_f32 v[42:43], v[60:61], v[46:47], v[42:43]
	v_lshlrev_b32_e32 v44, 16, v86
	v_and_b32_e32 v45, 0xffff0000, v86
	v_cvt_pk_bf16_f32 v55, v90, v91
	v_cvt_f32_fp8_sdwa v90, v195 src0_sel:BYTE_2
	v_cvt_f32_fp8_sdwa v91, v195 src0_sel:BYTE_3
	v_pk_fma_f32 v[44:45], v[88:89], v[62:63], v[44:45]
	v_lshlrev_b32_e32 v46, 16, v87
	v_and_b32_e32 v47, 0xffff0000, v87
	v_exp_f32_e32 v57, v36
	v_exp_f32_e32 v87, v37
	v_exp_f32_e32 v32, v32
	v_exp_f32_e32 v33, v33
	v_pk_mul_f32 v[38:39], v[38:39], v[138:139] op_sel_hi:[1,0]
	v_fmamk_f32 v37, v57, 0x41000000, v252
	v_fmamk_f32 v57, v87, 0x41000000, v252
	v_fmamk_f32 v32, v32, 0x41000000, v252
	v_pk_fma_f32 v[46:47], v[92:93], v[90:91], v[46:47]
	v_pk_mul_f32 v[34:35], v[34:35], v[138:139] op_sel_hi:[1,0]
	v_rcp_f32_e32 v87, v57
	v_exp_f32_e32 v57, v38
	v_rcp_f32_e32 v92, v32
	v_fmamk_f32 v32, v33, 0x41000000, v252
	v_exp_f32_e32 v89, v39
	v_rcp_f32_e32 v93, v32
	v_exp_f32_e32 v32, v34
	v_exp_f32_e32 v33, v35
	v_cvt_f32_fp8_e32 v36, v136
	v_rcp_f32_e32 v86, v37
	v_cvt_f32_fp8_sdwa v37, v136 src0_sel:BYTE_1
	v_fmamk_f32 v39, v57, 0x41000000, v252
	v_pk_mul_f32 v[58:59], v[40:41], v[40:41]
	v_cvt_f32_fp8_sdwa v38, v136 src0_sel:BYTE_2
	v_rcp_f32_e32 v88, v39
	v_cvt_f32_fp8_sdwa v39, v136 src0_sel:BYTE_3
	v_fmamk_f32 v57, v89, 0x41000000, v252
	v_pk_mul_f32 v[60:61], v[42:43], v[42:43]
	v_rcp_f32_e32 v89, v57
	v_cvt_f32_fp8_e32 v90, v137
	v_cvt_f32_fp8_sdwa v91, v137 src0_sel:BYTE_1
	v_fmamk_f32 v32, v32, 0x41000000, v252
	v_add_f32_e32 v57, v58, v59
	s_waitcnt vmcnt(13)
	v_mul_f32_e32 v128, 0xbfb8aa3b, v128
	v_pk_mul_f32 v[24:25], v[24:25], v[128:129] op_sel_hi:[1,0]
	v_cvt_f32_fp8_sdwa v94, v137 src0_sel:BYTE_2
	v_rcp_f32_e32 v112, v32
	v_cvt_f32_fp8_sdwa v95, v137 src0_sel:BYTE_3
	v_fmamk_f32 v32, v33, 0x41000000, v252
	v_add_f32_e32 v57, v60, v57
	v_pk_mul_f32 v[62:63], v[44:45], v[44:45]
	v_rcp_f32_e32 v113, v32
	v_lshlrev_b32_e32 v32, 16, v80
	v_and_b32_e32 v33, 0xffff0000, v80
	v_add_f32_e32 v57, v61, v57
	v_exp_f32_e32 v24, v24
	v_pk_fma_f32 v[32:33], v[86:87], v[36:37], v[32:33]
	v_lshlrev_b32_e32 v34, 16, v81
	v_and_b32_e32 v35, 0xffff0000, v81
	v_add_f32_e32 v57, v62, v57
	v_exp_f32_e32 v25, v25
	v_pk_mul_f32 v[84:85], v[46:47], v[46:47]
	v_pk_fma_f32 v[34:35], v[88:89], v[38:39], v[34:35]
	v_lshlrev_b32_e32 v36, 16, v82
	v_and_b32_e32 v37, 0xffff0000, v82
	v_add_f32_e32 v57, v63, v57
	v_pk_mul_f32 v[28:29], v[28:29], v[128:129] op_sel_hi:[1,0]
	v_pk_fma_f32 v[36:37], v[92:93], v[90:91], v[36:37]
	v_lshlrev_b32_e32 v38, 16, v83
	v_and_b32_e32 v39, 0xffff0000, v83
	v_add_f32_e32 v57, v84, v57
	v_pk_mul_f32 v[30:31], v[30:31], v[128:129] op_sel_hi:[1,0]
	v_pk_fma_f32 v[38:39], v[112:113], v[94:95], v[38:39]
	v_pk_mul_f32 v[80:81], v[32:33], v[32:33]
	v_add_f32_e32 v57, v85, v57
	v_exp_f32_e32 v58, v28
	v_fmamk_f32 v24, v24, 0x41000000, v252
	v_add_f32_e32 v57, v57, v80
	v_pk_mul_f32 v[26:27], v[26:27], v[128:129] op_sel_hi:[1,0]
	v_exp_f32_e32 v59, v29
	v_exp_f32_e32 v60, v30
	v_rcp_f32_e32 v80, v24
	v_fmamk_f32 v24, v25, 0x41000000, v252
	v_add_f32_e32 v57, v81, v57
	v_exp_f32_e32 v61, v31
	v_rcp_f32_e32 v81, v24
	v_exp_f32_e32 v24, v26
	v_fmamk_f32 v29, v58, 0x41000000, v252
	v_exp_f32_e32 v25, v27
	v_cvt_f32_fp8_e32 v28, v130
	v_rcp_f32_e32 v58, v29
	v_cvt_f32_fp8_sdwa v29, v130 src0_sel:BYTE_1
	v_fmamk_f32 v59, v59, 0x41000000, v252
	v_fmamk_f32 v31, v60, 0x41000000, v252
	v_pk_mul_f32 v[82:83], v[34:35], v[34:35]
	v_rcp_f32_e32 v59, v59
	v_cvt_f32_fp8_sdwa v30, v130 src0_sel:BYTE_2
	v_rcp_f32_e32 v60, v31
	v_cvt_f32_fp8_sdwa v31, v130 src0_sel:BYTE_3
	v_fmamk_f32 v61, v61, 0x41000000, v252
	v_pk_mul_f32 v[16:17], v[16:17], v[128:129] op_sel_hi:[1,0]
	v_add_f32_e32 v57, v82, v57
	v_rcp_f32_e32 v61, v61
	v_cvt_f32_fp8_e32 v62, v131
	v_cvt_f32_fp8_sdwa v63, v131 src0_sel:BYTE_1
	v_fmamk_f32 v24, v24, 0x41000000, v252
	v_add_f32_e32 v57, v83, v57
	v_cvt_f32_fp8_sdwa v82, v131 src0_sel:BYTE_2
	v_rcp_f32_e32 v84, v24
	v_cvt_f32_fp8_sdwa v83, v131 src0_sel:BYTE_3
	v_fmamk_f32 v24, v25, 0x41000000, v252
	v_exp_f32_e32 v16, v16
	v_rcp_f32_e32 v85, v24
	v_lshlrev_b32_e32 v24, 16, v76
	v_and_b32_e32 v25, 0xffff0000, v76
	v_exp_f32_e32 v17, v17
	v_pk_fma_f32 v[24:25], v[58:59], v[28:29], v[24:25]
	v_lshlrev_b32_e32 v26, 16, v77
	v_and_b32_e32 v27, 0xffff0000, v77
	v_pk_mul_f32 v[20:21], v[20:21], v[128:129] op_sel_hi:[1,0]
	v_pk_fma_f32 v[26:27], v[60:61], v[30:31], v[26:27]
	v_lshlrev_b32_e32 v28, 16, v78
	v_and_b32_e32 v29, 0xffff0000, v78
	v_pk_mul_f32 v[22:23], v[22:23], v[128:129] op_sel_hi:[1,0]
	v_pk_fma_f32 v[28:29], v[80:81], v[62:63], v[28:29]
	v_lshlrev_b32_e32 v30, 16, v79
	v_and_b32_e32 v31, 0xffff0000, v79
	v_exp_f32_e32 v78, v20
	v_fmamk_f32 v16, v16, 0x41000000, v252
	v_pk_fma_f32 v[30:31], v[84:85], v[82:83], v[30:31]
	v_pk_mul_f32 v[18:19], v[18:19], v[128:129] op_sel_hi:[1,0]
	v_exp_f32_e32 v79, v21
	v_exp_f32_e32 v80, v22
	v_rcp_f32_e32 v84, v16
	v_fmamk_f32 v16, v17, 0x41000000, v252
	v_exp_f32_e32 v81, v23
	v_rcp_f32_e32 v85, v16
	v_exp_f32_e32 v16, v18
	v_fmamk_f32 v21, v78, 0x41000000, v252
	v_exp_f32_e32 v17, v19
	v_pk_mul_f32 v[86:87], v[36:37], v[36:37]
	v_cvt_f32_fp8_e32 v20, v126
	v_rcp_f32_e32 v78, v21
	v_cvt_f32_fp8_sdwa v21, v126 src0_sel:BYTE_1
	v_fmamk_f32 v79, v79, 0x41000000, v252
	v_fmamk_f32 v23, v80, 0x41000000, v252
	v_add_f32_e32 v57, v86, v57
	v_pk_mul_f32 v[58:59], v[24:25], v[24:25]
	v_rcp_f32_e32 v79, v79
	v_cvt_f32_fp8_sdwa v22, v126 src0_sel:BYTE_2
	v_rcp_f32_e32 v80, v23
	v_cvt_f32_fp8_sdwa v23, v126 src0_sel:BYTE_3
	v_fmamk_f32 v81, v81, 0x41000000, v252
	v_pk_mul_f32 v[88:89], v[38:39], v[38:39]
	v_add_f32_e32 v57, v87, v57
	v_pk_mul_f32 v[60:61], v[26:27], v[26:27]
	v_rcp_f32_e32 v81, v81
	v_cvt_f32_fp8_e32 v82, v127
	v_cvt_f32_fp8_sdwa v83, v127 src0_sel:BYTE_1
	v_fmamk_f32 v16, v16, 0x41000000, v252
	v_add_f32_e32 v58, v58, v59
	v_add_f32_e32 v57, v88, v57
	v_cvt_f32_fp8_sdwa v86, v127 src0_sel:BYTE_2
	v_rcp_f32_e32 v88, v16
	v_cvt_f32_fp8_sdwa v87, v127 src0_sel:BYTE_3
	v_fmamk_f32 v16, v17, 0x41000000, v252
	v_add_f32_e32 v58, v60, v58
	v_add_f32_e32 v57, v89, v57
	v_pk_mul_f32 v[62:63], v[28:29], v[28:29]
	v_rcp_f32_e32 v89, v16
	v_lshlrev_b32_e32 v16, 16, v72
	v_and_b32_e32 v17, 0xffff0000, v72
	v_add_f32_e32 v58, v61, v58
	v_pk_fma_f32 v[16:17], v[78:79], v[20:21], v[16:17]
	v_lshlrev_b32_e32 v18, 16, v73
	v_and_b32_e32 v19, 0xffff0000, v73
	v_add_f32_e32 v58, v62, v58
	v_pk_mul_f32 v[76:77], v[30:31], v[30:31]
	v_pk_fma_f32 v[18:19], v[80:81], v[22:23], v[18:19]
	v_lshlrev_b32_e32 v20, 16, v74
	v_and_b32_e32 v21, 0xffff0000, v74
	v_add_f32_e32 v58, v63, v58
	v_pk_fma_f32 v[20:21], v[84:85], v[82:83], v[20:21]
	v_lshlrev_b32_e32 v22, 16, v75
	v_and_b32_e32 v23, 0xffff0000, v75
	v_add_f32_e32 v58, v76, v58
	v_pk_fma_f32 v[22:23], v[88:89], v[86:87], v[22:23]
	v_pk_mul_f32 v[72:73], v[16:17], v[16:17]
	v_add_f32_e32 v58, v77, v58
	v_add_f32_e32 v58, v58, v72
	v_pk_mul_f32 v[74:75], v[18:19], v[18:19]
	v_add_f32_e32 v58, v73, v58
	s_waitcnt vmcnt(12)
	v_mul_f32_e32 v118, 0xbfb8aa3b, v118
	v_pk_mul_f32 v[8:9], v[8:9], v[118:119] op_sel_hi:[1,0]
	v_add_f32_e32 v58, v74, v58
	v_pk_mul_f32 v[78:79], v[20:21], v[20:21]
	v_add_f32_e32 v58, v75, v58
	v_exp_f32_e32 v8, v8
	v_add_f32_e32 v58, v78, v58
	v_exp_f32_e32 v9, v9
	v_pk_mul_f32 v[80:81], v[22:23], v[22:23]
	v_add_f32_e32 v58, v79, v58
	v_pk_mul_f32 v[12:13], v[12:13], v[118:119] op_sel_hi:[1,0]
	v_add_f32_e32 v58, v80, v58
	v_pk_mul_f32 v[14:15], v[14:15], v[118:119] op_sel_hi:[1,0]
	v_add_f32_e32 v82, v81, v58
	v_exp_f32_e32 v58, v12
	v_fmamk_f32 v8, v8, 0x41000000, v252
	v_pk_mul_f32 v[10:11], v[10:11], v[118:119] op_sel_hi:[1,0]
	v_exp_f32_e32 v59, v13
	v_exp_f32_e32 v60, v14
	v_rcp_f32_e32 v72, v8
	v_fmamk_f32 v8, v9, 0x41000000, v252
	v_exp_f32_e32 v61, v15
	v_rcp_f32_e32 v73, v8
	v_exp_f32_e32 v8, v10
	v_fmamk_f32 v13, v58, 0x41000000, v252
	v_exp_f32_e32 v9, v11
	s_waitcnt vmcnt(9)
	v_cvt_f32_fp8_e32 v12, v124
	v_rcp_f32_e32 v58, v13
	v_cvt_f32_fp8_sdwa v13, v124 src0_sel:BYTE_1
	v_fmamk_f32 v59, v59, 0x41000000, v252
	v_fmamk_f32 v15, v60, 0x41000000, v252
	v_rcp_f32_e32 v59, v59
	v_cvt_f32_fp8_sdwa v14, v124 src0_sel:BYTE_2
	v_rcp_f32_e32 v60, v15
	v_cvt_f32_fp8_sdwa v15, v124 src0_sel:BYTE_3
	v_fmamk_f32 v61, v61, 0x41000000, v252
	v_pk_mul_f32 v[0:1], v[0:1], v[118:119] op_sel_hi:[1,0]
	v_rcp_f32_e32 v61, v61
	v_cvt_f32_fp8_e32 v62, v125
	v_cvt_f32_fp8_sdwa v63, v125 src0_sel:BYTE_1
	v_fmamk_f32 v8, v8, 0x41000000, v252
	v_cvt_f32_fp8_sdwa v74, v125 src0_sel:BYTE_2
	v_rcp_f32_e32 v76, v8
	v_cvt_f32_fp8_sdwa v75, v125 src0_sel:BYTE_3
	v_fmamk_f32 v8, v9, 0x41000000, v252
	v_exp_f32_e32 v0, v0
	v_rcp_f32_e32 v77, v8
	v_lshlrev_b32_e32 v8, 16, v68
	v_and_b32_e32 v9, 0xffff0000, v68
	v_exp_f32_e32 v1, v1
	v_pk_fma_f32 v[8:9], v[58:59], v[12:13], v[8:9]
	v_lshlrev_b32_e32 v10, 16, v69
	v_and_b32_e32 v11, 0xffff0000, v69
	v_pk_mul_f32 v[4:5], v[4:5], v[118:119] op_sel_hi:[1,0]
	v_pk_fma_f32 v[10:11], v[60:61], v[14:15], v[10:11]
	v_lshlrev_b32_e32 v12, 16, v70
	v_and_b32_e32 v13, 0xffff0000, v70
	v_pk_mul_f32 v[6:7], v[6:7], v[118:119] op_sel_hi:[1,0]
	v_pk_fma_f32 v[12:13], v[72:73], v[62:63], v[12:13]
	v_lshlrev_b32_e32 v14, 16, v71
	v_and_b32_e32 v15, 0xffff0000, v71
	v_exp_f32_e32 v70, v4
	v_fmamk_f32 v0, v0, 0x41000000, v252
	v_pk_fma_f32 v[14:15], v[76:77], v[74:75], v[14:15]
	v_pk_mul_f32 v[2:3], v[2:3], v[118:119] op_sel_hi:[1,0]
	v_exp_f32_e32 v71, v5
	v_exp_f32_e32 v72, v6
	v_rcp_f32_e32 v76, v0
	v_fmamk_f32 v0, v1, 0x41000000, v252
	v_exp_f32_e32 v73, v7
	v_rcp_f32_e32 v77, v0
	v_exp_f32_e32 v0, v2
	v_fmamk_f32 v5, v70, 0x41000000, v252
	v_exp_f32_e32 v1, v3
	s_waitcnt vmcnt(8)
	v_cvt_f32_fp8_e32 v4, v116
	v_rcp_f32_e32 v70, v5
	v_cvt_f32_fp8_sdwa v5, v116 src0_sel:BYTE_1
	v_fmamk_f32 v71, v71, 0x41000000, v252
	v_fmamk_f32 v7, v72, 0x41000000, v252
	v_pk_mul_f32 v[58:59], v[8:9], v[8:9]
	v_rcp_f32_e32 v71, v71
	v_cvt_f32_fp8_sdwa v6, v116 src0_sel:BYTE_2
	v_rcp_f32_e32 v72, v7
	v_cvt_f32_fp8_sdwa v7, v116 src0_sel:BYTE_3
	v_fmamk_f32 v73, v73, 0x41000000, v252
	v_pk_mul_f32 v[60:61], v[10:11], v[10:11]
	v_rcp_f32_e32 v73, v73
	v_cvt_f32_fp8_e32 v74, v117
	v_cvt_f32_fp8_sdwa v75, v117 src0_sel:BYTE_1
	v_fmamk_f32 v0, v0, 0x41000000, v252
	v_add_f32_e32 v58, v58, v59
	v_cvt_f32_fp8_sdwa v78, v117 src0_sel:BYTE_2
	v_rcp_f32_e32 v80, v0
	v_cvt_f32_fp8_sdwa v79, v117 src0_sel:BYTE_3
	v_fmamk_f32 v0, v1, 0x41000000, v252
	v_add_f32_e32 v58, v60, v58
	v_pk_mul_f32 v[62:63], v[12:13], v[12:13]
	v_rcp_f32_e32 v81, v0
	v_lshlrev_b32_e32 v0, 16, v64
	v_and_b32_e32 v1, 0xffff0000, v64
	v_add_f32_e32 v58, v61, v58
	v_pk_fma_f32 v[0:1], v[70:71], v[4:5], v[0:1]
	v_lshlrev_b32_e32 v2, 16, v65
	v_and_b32_e32 v3, 0xffff0000, v65
	v_add_f32_e32 v58, v62, v58
	v_pk_mul_f32 v[68:69], v[14:15], v[14:15]
	v_pk_fma_f32 v[2:3], v[72:73], v[6:7], v[2:3]
	v_lshlrev_b32_e32 v4, 16, v66
	v_and_b32_e32 v5, 0xffff0000, v66
	v_add_f32_e32 v58, v63, v58
	v_pk_fma_f32 v[4:5], v[76:77], v[74:75], v[4:5]
	v_lshlrev_b32_e32 v6, 16, v67
	v_and_b32_e32 v7, 0xffff0000, v67
	v_add_f32_e32 v58, v68, v58
	v_pk_fma_f32 v[6:7], v[80:81], v[78:79], v[6:7]
	v_pk_mul_f32 v[64:65], v[0:1], v[0:1]
	v_add_f32_e32 v58, v69, v58
	v_add_f32_e32 v58, v58, v64
	v_pk_mul_f32 v[66:67], v[2:3], v[2:3]
	v_add_f32_e32 v58, v65, v58
	v_add_f32_e32 v58, v66, v58
	v_pk_mul_f32 v[70:71], v[4:5], v[4:5]
	v_add_f32_e32 v58, v67, v58
	v_add_f32_e32 v58, v70, v58
	v_pk_mul_f32 v[72:73], v[6:7], v[6:7]
	v_add_f32_e32 v58, v71, v58
	v_add_f32_e32 v58, v72, v58
	v_add_f32_e32 v58, v73, v58
	ds_bpermute_b32 v90, v242, v57
	ds_bpermute_b32 v83, v242, v82
	ds_bpermute_b32 v63, v242, v58
	v_lshl_add_u64 v[64:65], s[40:41], 0, v[110:111]
	s_waitcnt lgkmcnt(2)
	v_add_f32_e32 v61, v57, v90
	s_waitcnt lgkmcnt(1)
	v_add_f32_e32 v59, v82, v83
	s_waitcnt lgkmcnt(0)
	v_add_f32_e32 v57, v58, v63
	ds_bpermute_b32 v62, v241, v61
	ds_bpermute_b32 v60, v241, v59
	ds_bpermute_b32 v58, v241, v57
	v_lshl_add_u64 v[64:65], v[168:169], 1, v[64:65]
	global_store_dwordx4 v[64:65], v[48:51], off
	global_store_dwordx4 v[64:65], v[52:55], off offset:256
	s_and_saveexec_b64 s[20:21], s[2:3]
	s_cbranch_execz .LBB0_1102
	v_lshl_add_u64 v[48:49], v[108:109], 2, s[0:1]
	global_atomic_add_f32 v[48:49], v56, off
